# speedup vs baseline: 1.0204x; 1.0078x over previous
.LBB3_6:
	v_mov_b32_e32 v64, v217
	v_mov_b32_e32 v65, v218
	v_mov_b32_e32 v66, v219
	v_mov_b32_e32 v67, v220
	s_andn2_b64 vcc, exec, s[0:1]
	ds_read_b128 v[32:35], v64 offset:0
	ds_read_b128 v[36:39], v65 offset:0
	ds_read_b128 v[40:43], v66 offset:0
	ds_read_b128 v[44:47], v67 offset:0
	ds_read_b128 v[48:51], v64 offset:128
	ds_read_b128 v[52:55], v65 offset:128
	ds_read_b128 v[56:59], v66 offset:128
	ds_read_b128 v[60:63], v67 offset:128
	s_nop 0
	s_waitcnt lgkmcnt(0)
	s_nop 0
	s_nop 0
	v_accvgpr_write_b32 a[128], v32
	v_accvgpr_write_b32 a[129], v33
	v_accvgpr_write_b32 a[130], v34
	v_accvgpr_write_b32 a[131], v35
	v_accvgpr_write_b32 a[132], v36
	v_accvgpr_write_b32 a[133], v37
	v_accvgpr_write_b32 a[134], v38
	v_accvgpr_write_b32 a[135], v39
	v_accvgpr_write_b32 a[136], v40
	v_accvgpr_write_b32 a[137], v41
	v_accvgpr_write_b32 a[138], v42
	v_accvgpr_write_b32 a[139], v43
	v_accvgpr_write_b32 a[140], v44
	v_accvgpr_write_b32 a[141], v45
	v_accvgpr_write_b32 a[142], v46
	v_accvgpr_write_b32 a[143], v47
	v_accvgpr_write_b32 a[144], v48
	v_accvgpr_write_b32 a[145], v49
	v_accvgpr_write_b32 a[146], v50
	v_accvgpr_write_b32 a[147], v51
	v_accvgpr_write_b32 a[148], v52
	v_accvgpr_write_b32 a[149], v53
	v_accvgpr_write_b32 a[150], v54
	v_accvgpr_write_b32 a[151], v55
	v_accvgpr_write_b32 a[152], v56
	v_accvgpr_write_b32 a[153], v57
	v_accvgpr_write_b32 a[154], v58
	v_accvgpr_write_b32 a[155], v59
	s_nop 0
	v_accvgpr_write_b32 a[156], v60
	v_accvgpr_write_b32 a[157], v61
	v_accvgpr_write_b32 a[158], v62
	v_accvgpr_write_b32 a[159], v63
	ds_read_b128 v[32:35], v64 offset:8192
	ds_read_b128 v[36:39], v65 offset:8192
	ds_read_b128 v[40:43], v66 offset:8192
	ds_read_b128 v[44:47], v67 offset:8192
	ds_read_b128 v[48:51], v64 offset:8320
	ds_read_b128 v[52:55], v65 offset:8320
	ds_read_b128 v[56:59], v66 offset:8320
	ds_read_b128 v[60:63], v67 offset:8320
	s_nop 0
	s_waitcnt lgkmcnt(0)
	s_nop 0
	s_nop 0
	v_accvgpr_write_b32 a[160], v32
	v_accvgpr_write_b32 a[161], v33
	v_accvgpr_write_b32 a[162], v34
	v_accvgpr_write_b32 a[163], v35
	s_nop 0
	v_accvgpr_write_b32 a[164], v36
	v_accvgpr_write_b32 a[165], v37
	v_accvgpr_write_b32 a[166], v38
	v_accvgpr_write_b32 a[167], v39
	s_nop 0
	v_accvgpr_write_b32 a[168], v40
	v_accvgpr_write_b32 a[169], v41
	v_accvgpr_write_b32 a[170], v42
	v_accvgpr_write_b32 a[171], v43
	s_nop 0
	v_accvgpr_write_b32 a[172], v44
	v_accvgpr_write_b32 a[173], v45
	v_accvgpr_write_b32 a[174], v46
	v_accvgpr_write_b32 a[175], v47
	s_nop 0
	v_accvgpr_write_b32 a[176], v48
	v_accvgpr_write_b32 a[177], v49
	v_accvgpr_write_b32 a[178], v50
	v_accvgpr_write_b32 a[179], v51
	s_nop 0
	v_accvgpr_write_b32 a[180], v52
	v_accvgpr_write_b32 a[181], v53
	v_accvgpr_write_b32 a[182], v54
	v_accvgpr_write_b32 a[183], v55
	s_nop 0
	v_accvgpr_write_b32 a[184], v56
	v_accvgpr_write_b32 a[185], v57
	v_accvgpr_write_b32 a[186], v58
	v_accvgpr_write_b32 a[187], v59
	s_nop 0
	v_accvgpr_write_b32 a[188], v60
	v_accvgpr_write_b32 a[189], v61
	v_accvgpr_write_b32 a[190], v62
	v_accvgpr_write_b32 a[191], v63
	s_waitcnt vmcnt(0)
	s_barrier
	s_cbranch_vccnz .LBB3_8
	ds_read_b128 a[192:195], v206 offset:0
	s_nop 0
	ds_read_b128 a[196:199], v207 offset:0
	s_nop 0
	ds_read_b128 a[200:203], v208 offset:0
	s_nop 0
	ds_read_b128 a[204:207], v209 offset:0
	s_nop 0
	ds_read_b128 a[208:211], v206 offset:128
	s_nop 0
	ds_read_b128 a[212:215], v207 offset:128
	s_nop 0
	ds_read_b128 a[216:219], v208 offset:128
	s_nop 0
	ds_read_b128 a[220:223], v209 offset:128
	s_nop 0
	ds_read_b128 a[224:227], v206 offset:8192
	s_nop 0
	ds_read_b128 a[228:231], v207 offset:8192
	s_nop 0
	ds_read_b128 a[232:235], v208 offset:8192
	s_nop 0
	ds_read_b128 a[236:239], v209 offset:8192
	s_nop 0
	ds_read_b128 a[240:243], v206 offset:8320
	s_nop 0
	ds_read_b128 a[244:247], v207 offset:8320
	s_nop 0
	ds_read_b128 a[248:251], v208 offset:8320
	s_nop 0
	ds_read_b128 a[252:255], v209 offset:8320

.LBB3_21:
	s_add_u32 s30, s28, s39
	s_addc_u32 s31, s29, 0
	v_cmp_lt_u64_e32 vcc, s[30:31], v[202:203]
	s_and_b64 s[0:1], vcc, exec
	s_cselect_b32 s0, s30, s28
	s_and_b32 s1, s0, 15
	s_lshl_b32 s12, s0, 4
	s_lshr_b32 s0, s0, 3
	s_and_b32 s0, s0, 0x1ffffff0
	s_or_b32 s24, s1, s0
	s_and_b32 s12, s12, 0x700
	s_lshl_b64 s[34:35], s[24:25], 19
	v_exp_f32_e32 v48, v48
	v_exp_f32_e32 v49, v49
	s_add_u32 s16, s6, s34
	v_mfma_f32_32x32x16_f16 v[112:127], a[192:195], a[128:131], v[16:31]
	ds_read_b64_tr_b16 v[180:181], v225 offset:0
	v_or_b32_e32 v64, s12, v215
	s_addc_u32 s0, s7, s35
	s_and_b32 s17, s0, 0xffff
	v_readfirstlane_b32 s24, v64
	s_mov_b32 s12, s16
	s_mov_b32 s13, s17
	v_cvt_pk_f16_f32 v164, v128, v129
	v_exp_f32_e32 v50, v50
	v_exp_f32_e32 v51, v51
	v_mfma_f32_32x32x16_f16 v[96:111], a[192:195], a[160:163], v[0:15]
	ds_read_b64_tr_b16 v[182:183], v225 offset:0x800
	v_cvt_pk_f16_f32 v165, v130, v131
	v_exp_f32_e32 v232, v52
	v_exp_f32_e32 v233, v53
	v_mfma_f32_32x32x16_f16 v[80:95], a[224:227], a[128:131], v[16:31]
	ds_read_b64_tr_b16 v[184:185], v225 offset:0x200
	v_cvt_pk_f16_f32 v166, v132, v133
	v_mfma_f32_32x32x16_f16 v[64:79], a[224:227], a[160:163], v[0:15]
	ds_read_b64_tr_b16 v[186:187], v225 offset:0xa00
	ds_read_b64_tr_b16 v[176:177], v225 offset:0x400
	v_exp_f32_e32 v244, v54
	v_exp_f32_e32 v245, v55
	v_cvt_pk_f16_f32 v167, v134, v135
	v_exp_f32_e32 v198, v56
	v_exp_f32_e32 v199, v57
	v_mfma_f32_32x32x16_f16 v[112:127], a[196:199], a[132:135], v[112:127]
	ds_read_b64_tr_b16 v[178:179], v225 offset:0xc00
	v_cvt_pk_f16_f32 v128, v136, v137
	v_exp_f32_e32 v234, v58
	v_exp_f32_e32 v235, v59
	v_mfma_f32_32x32x16_f16 v[96:111], a[196:199], a[164:167], v[96:111]
	ds_read_b64_tr_b16 v[188:189], v225 offset:0x600
	v_cvt_pk_f16_f32 v129, v138, v139
	v_exp_f32_e32 v236, v60
	v_exp_f32_e32 v237, v61
	v_mfma_f32_32x32x16_f16 v[80:95], a[228:231], a[132:135], v[80:95]
	ds_read_b64_tr_b16 v[190:191], v225 offset:0xe00
	v_cvt_pk_f16_f32 v130, v140, v141
	v_mfma_f32_32x32x16_f16 v[64:79], a[228:231], a[164:167], v[64:79]
	ds_read_b64_tr_b16 v[172:173], v225 offset:0x1000
	v_exp_f32_e32 v238, v62
	v_exp_f32_e32 v239, v63
	ds_read_b64_tr_b16 v[174:175], v225 offset:0x1800
	v_cvt_pk_f16_f32 v131, v142, v143
	v_exp_f32_e32 v141, v32
	v_exp_f32_e32 v142, v33
	v_mfma_f32_32x32x16_f16 v[112:127], a[200:203], a[136:139], v[112:127]
	ds_read_b64_tr_b16 v[168:169], v225 offset:0x1200
	v_cvt_pk_f16_f32 v192, v144, v145
	v_exp_f32_e32 v143, v34
	v_mfma_f32_32x32x16_f16 v[96:111], a[200:203], a[168:171], v[96:111]
	ds_read_b64_tr_b16 v[170:171], v225 offset:0x1a00
	v_exp_f32_e32 v246, v35
	v_cvt_pk_f16_f32 v193, v146, v147
	v_mfma_f32_32x32x16_f16 v[80:95], a[232:235], a[136:139], v[80:95]
	ds_read_b64_tr_b16 v[160:161], v225 offset:0x1400
	v_exp_f32_e32 v247, v36
	v_exp_f32_e32 v248, v37
	v_cvt_pk_f16_f32 v194, v148, v149
	v_mfma_f32_32x32x16_f16 v[64:79], a[232:235], a[168:171], v[64:79]
	ds_read_b64_tr_b16 v[162:163], v225 offset:0x1c00
	ds_read_b64_tr_b16 v[136:137], v225 offset:0x1600
	v_exp_f32_e32 v249, v38
	v_exp_f32_e32 v250, v39
	v_cvt_pk_f16_f32 v195, v150, v151
	v_exp_f32_e32 v148, v40
	v_exp_f32_e32 v149, v41
	v_mfma_f32_32x32x16_f16 v[112:127], a[204:207], a[140:143], v[112:127]
	ds_read_b64_tr_b16 v[138:139], v225 offset:0x1e00
	v_cvt_pk_f16_f32 v144, v152, v153
	v_exp_f32_e32 v150, v42
	v_exp_f32_e32 v151, v43
	v_mfma_f32_32x32x16_f16 v[96:111], a[204:207], a[172:175], v[96:111]
	ds_read_b64_tr_b16 v[132:133], v225 offset:0x2000
	v_cvt_pk_f16_f32 v145, v154, v155
	v_exp_f32_e32 v152, v44
	v_exp_f32_e32 v153, v45
	v_mfma_f32_32x32x16_f16 v[80:95], a[236:239], a[140:143], v[80:95]
	ds_read_b64_tr_b16 v[134:135], v225 offset:0x2800
	v_cvt_pk_f16_f32 v146, v156, v157
	v_mfma_f32_32x32x16_f16 v[64:79], a[236:239], a[172:175], v[64:79]
	ds_read_b64_tr_b16 v[60:61], v225 offset:0x2200
	v_exp_f32_e32 v154, v46
	v_exp_f32_e32 v155, v47
	ds_read_b64_tr_b16 v[62:63], v225 offset:0x2a00
	v_cvt_pk_f16_f32 v147, v158, v159
	s_mov_b32 s0, s33
	v_mfma_f32_32x32x16_f16 v[112:127], a[208:211], a[144:147], v[112:127]
	ds_read_b64_tr_b16 v[56:57], v225 offset:0x2400
	v_cvt_pk_f16_f32 v52, v48, v49
	v_add_f32_e32 v32, v241, v48
	v_add_f32_e32 v33, v240, v49
	s_mov_b32 s1, s36
	v_mfma_f32_32x32x16_f16 v[96:111], a[208:211], a[176:179], v[96:111]
	ds_read_b64_tr_b16 v[58:59], v225 offset:0x2c00
	v_cvt_pk_f16_f32 v53, v50, v51
	v_add_f32_e32 v32, v32, v50
	v_add_f32_e32 v33, v33, v51
	s_mov_b32 s22, s41
	v_mfma_f32_32x32x16_f16 v[80:95], a[240:243], a[144:147], v[80:95]
	ds_read_b64_tr_b16 v[48:49], v225 offset:0x2600
	v_cvt_pk_f16_f32 v54, v232, v233
	v_add_f32_e32 v32, v32, v232
	v_add_f32_e32 v33, v33, v233
	s_mov_b32 s23, s68
	v_mfma_f32_32x32x16_f16 v[64:79], a[240:243], a[176:179], v[64:79]
	ds_read_b64_tr_b16 v[50:51], v225 offset:0x2e00
	ds_read_b64_tr_b16 v[44:45], v225 offset:0x3000
	v_cvt_pk_f16_f32 v55, v244, v245
	v_add_f32_e32 v32, v32, v244
	v_add_f32_e32 v33, v33, v245
	s_mov_b32 s29, s43
	v_mfma_f32_32x32x16_f16 v[112:127], a[212:215], a[148:151], v[112:127]
	ds_read_b64_tr_b16 v[46:47], v225 offset:0x3800
	v_add_f32_e32 v32, v32, v198
	v_add_f32_e32 v33, v33, v199
	s_mov_b32 s91, s69
	v_mfma_f32_32x32x16_f16 v[96:111], a[212:215], a[180:183], v[96:111]
	ds_read_b64_tr_b16 v[40:41], v225 offset:0x3200
	v_add_f32_e32 v32, v32, v234
	v_add_f32_e32 v33, v33, v235
	s_mov_b32 s92, s45
	v_mfma_f32_32x32x16_f16 v[80:95], a[244:247], a[148:151], v[80:95]
	ds_read_b64_tr_b16 v[42:43], v225 offset:0x3a00
	v_add_f32_e32 v32, v32, v236
	v_add_f32_e32 v33, v33, v237
	s_mov_b32 s94, s70
	v_mfma_f32_32x32x16_f16 v[64:79], a[244:247], a[180:183], v[64:79]
	ds_read_b64_tr_b16 v[36:37], v225 offset:0x3400
	ds_read_b64_tr_b16 v[38:39], v225 offset:0x3c00
	v_add_f32_e32 v156, v32, v238
	v_add_f32_e32 v157, v33, v239
	s_mov_b32 s93, s47
	v_mfma_f32_32x32x16_f16 v[112:127], a[216:219], a[152:155], v[112:127]
	ds_read_b64_tr_b16 v[32:33], v225 offset:0x3600
	v_cvt_pk_f16_f32 v140, v141, v142
	v_add_f32_e32 v158, v242, v141
	v_add_f32_e32 v142, v243, v142
	s_mov_b32 s95, s71
	v_mfma_f32_32x32x16_f16 v[96:111], a[216:219], a[184:187], v[96:111]
	ds_read_b64_tr_b16 v[34:35], v225 offset:0x3e00
	v_cvt_pk_f16_f32 v141, v143, v246
	v_add_f32_e32 v143, v158, v143
	v_add_f32_e32 v158, v142, v246
	v_mfma_f32_32x32x16_f16 v[80:95], a[248:251], a[152:155], v[80:95]
	s_mov_b32 s96, s49
	v_cvt_pk_f16_f32 v142, v247, v248
	v_add_f32_e32 v159, v143, v247
	v_add_f32_e32 v158, v158, v248
	v_mfma_f32_32x32x16_f16 v[64:79], a[248:251], a[184:187], v[64:79]
	s_mov_b32 s97, s72
	v_cvt_pk_f16_f32 v143, v249, v250
	v_add_f32_e32 v159, v159, v249
	v_add_f32_e32 v158, v158, v250
	v_mfma_f32_32x32x16_f16 v[112:127], a[220:223], a[156:159], v[112:127]
	s_mov_b32 s98, s51
	v_add_f32_e32 v159, v159, v148
	v_add_f32_e32 v158, v158, v149
	v_mfma_f32_32x32x16_f16 v[96:111], a[220:223], a[188:191], v[96:111]
	s_mov_b32 s99, s73
	v_add_f32_e32 v159, v159, v150
	v_add_f32_e32 v158, v158, v151
	v_mfma_f32_32x32x16_f16 v[80:95], a[252:255], a[156:159], v[80:95]
	s_mov_b32 vcc_lo, s53
	v_add_f32_e32 v159, v159, v152
	v_add_f32_e32 v158, v158, v153
	v_mfma_f32_32x32x16_f16 v[64:79], a[252:255], a[188:191], v[64:79]
	s_mov_b32 vcc_hi, s74
	v_add_f32_e32 v159, v159, v154
	v_add_f32_e32 v158, v158, v155
	s_nop 0
	s_nop 4
	v_add_f32_e32 v156, v156, v157
	s_waitcnt vmcnt(0) lgkmcnt(0)
	s_barrier
	s_nop 0
	v_mov_b32_e32 v157, v156
	s_nop 1
	v_permlane32_swap_b32_e32 v156, v157
	v_add_f32_e32 v156, v156, v157
	s_nop 0
	v_add_f32_e32 v233, v197, v156
	v_add_f32_e32 v156, v159, v158
	s_nop 0
	v_mov_b32_e32 v157, v156
	s_nop 1
	v_permlane32_swap_b32_e32 v156, v157
	v_add_f32_e32 v156, v156, v157
	s_nop 0
	v_add_f32_e32 v232, v196, v156
	s_nop 1
	v_mfma_f32_32x32x16_f16 a[0:15], v[180:183], v[164:167], a[0:15]
	s_nop 0
	v_mfma_f32_32x32x16_f16 a[16:31], v[180:183], v[192:195], a[16:31]
	ds_read_b128 a[192:195], v221 offset:0
	s_nop 0
	v_mfma_f32_32x32x16_f16 a[32:47], v[184:187], v[164:167], a[32:47]
	ds_read_b128 a[196:199], v222 offset:0
	s_nop 0
	v_mfma_f32_32x32x16_f16 a[48:63], v[184:187], v[192:195], a[48:63]
	ds_read_b128 a[200:203], v223 offset:0
	s_nop 0
	v_mfma_f32_32x32x16_f16 a[64:79], v[176:179], v[164:167], a[64:79]
	s_mov_b32 s22, s18
	s_mov_b32 s23, s19
	s_mov_b32 m0, s93
	s_nop 0
	buffer_load_dwordx4 v213, s[20:23], s95 offen lds
	ds_read_b128 a[204:207], v224 offset:0
	v_mfma_f32_32x32x16_f16 a[80:95], v[176:179], v[192:195], a[80:95]
	s_nop 0
	s_mov_b32 m0, s96
	s_nop 0
	buffer_load_dwordx4 v213, s[20:23], s97 offen lds
	ds_read_b128 a[208:211], v221 offset:128
	v_mfma_f32_32x32x16_f16 a[96:111], v[188:191], v[164:167], a[96:111]
	s_nop 0
	s_mov_b32 m0, s98
	s_nop 0
	buffer_load_dwordx4 v213, s[20:23], s99 offen lds
	ds_read_b128 a[212:215], v222 offset:128
	v_mfma_f32_32x32x16_f16 a[112:127], v[188:191], v[192:195], a[112:127]
	s_nop 0
	s_mov_b32 m0, vcc_lo
	s_nop 0
	buffer_load_dwordx4 v213, s[20:23], vcc_hi offen lds
	ds_read_b128 a[216:219], v223 offset:128
	v_mfma_f32_32x32x16_f16 a[0:15], v[172:175], v[128:131], a[0:15]
	s_nop 0
	ds_read_b128 a[220:223], v224 offset:128
	v_max3_f32 v156, v112, v113, v80
	v_max3_f32 v157, v114, v115, v81
	s_nop 0
	v_max3_f32 v156, v156, v82, v83
	v_mfma_f32_32x32x16_f16 a[16:31], v[172:175], v[144:147], a[16:31]
	ds_read_b128 a[224:227], v221 offset:8192
	s_nop 0
	v_max3_f32 v156, v156, v116, v117
	v_max3_f32 v157, v157, v118, v119
	s_nop 0
	v_max3_f32 v156, v156, v84, v85
	v_max3_f32 v157, v157, v86, v87
	v_mfma_f32_32x32x16_f16 a[32:47], v[168:171], v[128:131], a[32:47]
	ds_read_b128 a[228:231], v222 offset:8192
	s_nop 0
	v_max3_f32 v156, v156, v120, v121
	v_max3_f32 v157, v157, v122, v123
	s_nop 0
	v_max3_f32 v156, v156, v88, v89
	v_max3_f32 v157, v157, v90, v91
	v_mfma_f32_32x32x16_f16 a[48:63], v[168:171], v[144:147], a[48:63]
	ds_read_b128 a[232:235], v223 offset:8192
	s_nop 0
	v_max3_f32 v156, v156, v124, v125
	v_max3_f32 v157, v157, v126, v127
	s_nop 0
	v_max3_f32 v156, v156, v92, v93
	v_max3_f32 v157, v157, v94, v95
	v_mfma_f32_32x32x16_f16 a[64:79], v[160:163], v[128:131], a[64:79]
	ds_read_b128 a[236:239], v224 offset:8192
	v_max3_f32 v158, v96, v97, v64
	v_max3_f32 v159, v98, v99, v65
	s_nop 0
	v_max3_f32 v158, v158, v66, v67
	v_mfma_f32_32x32x16_f16 a[80:95], v[160:163], v[144:147], a[80:95]
	ds_read_b128 a[240:243], v221 offset:8320
	s_nop 0
	v_max3_f32 v158, v158, v100, v101
	v_max3_f32 v159, v159, v102, v103
	s_nop 0
	v_max3_f32 v158, v158, v68, v69
	v_max3_f32 v159, v159, v70, v71
	v_mfma_f32_32x32x16_f16 a[96:111], v[136:139], v[128:131], a[96:111]
	ds_read_b128 a[244:247], v222 offset:8320
	s_nop 0
	v_max3_f32 v128, v158, v104, v105
	v_max3_f32 v129, v159, v106, v107
	s_nop 0
	v_max3_f32 v128, v128, v72, v73
	v_max3_f32 v129, v129, v74, v75
	v_mfma_f32_32x32x16_f16 a[112:127], v[136:139], v[144:147], a[112:127]
	ds_read_b128 a[248:251], v223 offset:8320
	s_nop 0
	v_max3_f32 v128, v128, v108, v109
	v_max3_f32 v129, v129, v110, v111
	s_nop 0
	v_max3_f32 v128, v128, v76, v77
	v_max3_f32 v130, v129, v78, v79
	v_mfma_f32_32x32x16_f16 a[0:15], v[132:135], v[52:55], a[0:15]
	ds_read_b128 a[252:255], v224 offset:8320
	v_max_f32_e32 v129, v156, v157
	s_nop 0
	v_mov_b32_e32 v131, v129
	s_nop 1
	v_permlane32_swap_b32_e32 v129, v131
	v_max_f32_e32 v129, v129, v131
	v_mfma_f32_32x32x16_f16 a[16:31], v[132:135], v[140:143], a[16:31]
	v_max_f32_e32 v128, v128, v130
	s_nop 0
	v_mov_b32_e32 v130, v128
	s_nop 1
	v_permlane32_swap_b32_e32 v128, v130
	v_max_f32_e32 v128, v128, v130
	v_max_f32_e32 v130, v129, v129
	v_max_f32_e32 v131, v128, v128
	v_max_f32_e32 v130, v130, v131
	v_mfma_f32_32x32x16_f16 a[32:47], v[60:63], v[52:55], a[32:47]
	v_cmp_lt_f32_e32 vcc, s79, v130
	s_cmp_lg_u64 vcc, 0
	s_cselect_b64 s[0:1], -1, 0
	s_cbranch_vccnz .LBB3_28

.LBB3_23:
	s_add_u32 s12, s8, s34
	s_waitcnt lgkmcnt(0)
	s_addc_u32 s0, s9, s35
	s_and_b32 s13, s0, 0xffff
	v_mfma_f32_32x32x16_f16 v[112:127], a[192:195], a[128:131], v[16:31]
	ds_read_b64_tr_b16 v[184:185], v210 offset:0
	v_exp_f32_e32 v242, v80
	v_exp_f32_e32 v243, v81
	v_cvt_pk_f16_f32 v168, v128, v129
	v_exp_f32_e32 v82, v82
	v_exp_f32_e32 v83, v83
	v_mfma_f32_32x32x16_f16 v[96:111], a[192:195], a[160:163], v[0:15]
	ds_read_b64_tr_b16 v[186:187], v210 offset:0x800
	v_cvt_pk_f16_f32 v169, v130, v131
	v_exp_f32_e32 v84, v84
	v_exp_f32_e32 v85, v85
	v_mfma_f32_32x32x16_f16 v[48:63], a[224:227], a[128:131], v[16:31]
	ds_read_b64_tr_b16 v[188:189], v210 offset:0x200
	v_cvt_pk_f16_f32 v170, v132, v133
	v_mfma_f32_32x32x16_f16 v[32:47], a[224:227], a[160:163], v[0:15]
	ds_read_b64_tr_b16 v[190:191], v210 offset:0xa00
	v_exp_f32_e32 v86, v86
	v_exp_f32_e32 v87, v87
	ds_read_b64_tr_b16 v[180:181], v210 offset:0x400
	v_cvt_pk_f16_f32 v171, v134, v135
	v_exp_f32_e32 v80, v88
	v_exp_f32_e32 v81, v89
	v_mfma_f32_32x32x16_f16 v[112:127], a[196:199], a[132:135], v[112:127]
	ds_read_b64_tr_b16 v[182:183], v210 offset:0xc00
	v_cvt_pk_f16_f32 v160, v136, v137
	v_exp_f32_e32 v90, v90
	v_exp_f32_e32 v91, v91
	v_mfma_f32_32x32x16_f16 v[96:111], a[196:199], a[164:167], v[96:111]
	ds_read_b64_tr_b16 v[192:193], v210 offset:0x600
	v_cvt_pk_f16_f32 v161, v138, v139
	v_exp_f32_e32 v234, v92
	v_exp_f32_e32 v235, v93
	v_mfma_f32_32x32x16_f16 v[48:63], a[228:231], a[132:135], v[48:63]
	ds_read_b64_tr_b16 v[194:195], v210 offset:0xe00
	v_cvt_pk_f16_f32 v162, v140, v141
	v_mfma_f32_32x32x16_f16 v[32:47], a[228:231], a[164:167], v[32:47]
	ds_read_b64_tr_b16 v[176:177], v210 offset:0x1000
	v_exp_f32_e32 v236, v94
	v_exp_f32_e32 v237, v95
	ds_read_b64_tr_b16 v[178:179], v210 offset:0x1800
	v_cvt_pk_f16_f32 v163, v142, v143
	v_exp_f32_e32 v130, v64
	v_exp_f32_e32 v131, v65
	v_mfma_f32_32x32x16_f16 v[112:127], a[200:203], a[136:139], v[112:127]
	ds_read_b64_tr_b16 v[172:173], v210 offset:0x1200
	v_cvt_pk_f16_f32 v196, v144, v145
	v_exp_f32_e32 v138, v66
	v_exp_f32_e32 v139, v67
	v_mfma_f32_32x32x16_f16 v[96:111], a[200:203], a[168:171], v[96:111]
	ds_read_b64_tr_b16 v[174:175], v210 offset:0x1a00
	v_cvt_pk_f16_f32 v197, v146, v147
	v_mfma_f32_32x32x16_f16 v[48:63], a[232:235], a[136:139], v[48:63]
	ds_read_b64_tr_b16 v[164:165], v210 offset:0x1400
	v_exp_f32_e32 v244, v68
	v_exp_f32_e32 v245, v69
	v_cvt_pk_f16_f32 v198, v148, v149
	v_mfma_f32_32x32x16_f16 v[32:47], a[232:235], a[168:171], v[32:47]
	ds_read_b64_tr_b16 v[166:167], v210 offset:0x1c00
	ds_read_b64_tr_b16 v[144:145], v210 offset:0x1600
	v_exp_f32_e32 v246, v70
	v_exp_f32_e32 v247, v71
	v_cvt_pk_f16_f32 v199, v150, v151
	v_exp_f32_e32 v64, v72
	v_exp_f32_e32 v65, v73
	v_mfma_f32_32x32x16_f16 v[112:127], a[204:207], a[140:143], v[112:127]
	ds_read_b64_tr_b16 v[146:147], v210 offset:0x1e00
	v_cvt_pk_f16_f32 v148, v152, v153
	v_exp_f32_e32 v70, v74
	v_exp_f32_e32 v71, v75
	v_mfma_f32_32x32x16_f16 v[96:111], a[204:207], a[172:175], v[96:111]
	ds_read_b64_tr_b16 v[140:141], v210 offset:0x2000
	v_cvt_pk_f16_f32 v149, v154, v155
	v_exp_f32_e32 v152, v76
	v_exp_f32_e32 v153, v77
	v_mfma_f32_32x32x16_f16 v[48:63], a[236:239], a[140:143], v[48:63]
	ds_read_b64_tr_b16 v[142:143], v210 offset:0x2800
	v_cvt_pk_f16_f32 v150, v156, v157
	v_mfma_f32_32x32x16_f16 v[32:47], a[236:239], a[172:175], v[32:47]
	ds_read_b64_tr_b16 v[66:67], v210 offset:0x2200
	v_exp_f32_e32 v154, v78
	v_exp_f32_e32 v155, v79
	ds_read_b64_tr_b16 v[68:69], v210 offset:0x2a00
	v_cvt_pk_f16_f32 v151, v158, v159
	s_mov_b32 s0, s55
	v_mfma_f32_32x32x16_f16 v[112:127], a[208:211], a[144:147], v[112:127]
	ds_read_b64_tr_b16 v[132:133], v210 offset:0x2400
	v_cvt_pk_f16_f32 v72, v242, v243
	v_add_f32_e32 v74, v239, v242
	v_add_f32_e32 v75, v238, v243
	s_mov_b32 s1, s48
	v_mfma_f32_32x32x16_f16 v[96:111], a[208:211], a[176:179], v[96:111]
	ds_read_b64_tr_b16 v[134:135], v210 offset:0x2c00
	v_cvt_pk_f16_f32 v73, v82, v83
	v_add_f32_e32 v78, v74, v82
	v_add_f32_e32 v75, v75, v83
	s_mov_b32 s20, s57
	v_mfma_f32_32x32x16_f16 v[48:63], a[240:243], a[144:147], v[48:63]
	ds_read_b64_tr_b16 v[76:77], v210 offset:0x2600
	v_cvt_pk_f16_f32 v74, v84, v85
	v_add_f32_e32 v84, v78, v84
	v_add_f32_e32 v85, v75, v85
	s_mov_b32 s21, s75
	v_mfma_f32_32x32x16_f16 v[32:47], a[240:243], a[176:179], v[32:47]
	ds_read_b64_tr_b16 v[78:79], v210 offset:0x2e00
	ds_read_b64_tr_b16 v[82:83], v210 offset:0x3000
	v_cvt_pk_f16_f32 v75, v86, v87
	v_add_f32_e32 v86, v84, v86
	v_add_f32_e32 v87, v85, v87
	s_mov_b32 s22, s59
	v_mfma_f32_32x32x16_f16 v[112:127], a[212:215], a[148:151], v[112:127]
	ds_read_b64_tr_b16 v[84:85], v210 offset:0x3800
	v_add_f32_e32 v88, v86, v80
	v_add_f32_e32 v89, v87, v81
	s_mov_b32 s23, s52
	v_mfma_f32_32x32x16_f16 v[96:111], a[212:215], a[180:183], v[96:111]
	ds_read_b64_tr_b16 v[86:87], v210 offset:0x3200
	v_add_f32_e32 v92, v88, v90
	v_add_f32_e32 v93, v89, v91
	s_mov_b32 s29, s61
	v_mfma_f32_32x32x16_f16 v[48:63], a[244:247], a[148:151], v[48:63]
	ds_read_b64_tr_b16 v[88:89], v210 offset:0x3a00
	v_add_f32_e32 v128, v92, v234
	v_add_f32_e32 v129, v93, v235
	s_mov_b32 s91, s76
	v_mfma_f32_32x32x16_f16 v[32:47], a[244:247], a[180:183], v[32:47]
	ds_read_b64_tr_b16 v[92:93], v210 offset:0x3400
	ds_read_b64_tr_b16 v[94:95], v210 offset:0x3c00
	v_add_f32_e32 v156, v128, v236
	v_add_f32_e32 v157, v129, v237
	s_mov_b32 s92, s38
	v_mfma_f32_32x32x16_f16 v[112:127], a[216:219], a[152:155], v[112:127]
	ds_read_b64_tr_b16 v[128:129], v210 offset:0x3600
	v_cvt_pk_f16_f32 v136, v130, v131
	v_add_f32_e32 v158, v240, v130
	v_add_f32_e32 v159, v241, v131
	s_mov_b32 s93, s36
	v_mfma_f32_32x32x16_f16 v[96:111], a[216:219], a[184:187], v[96:111]
	ds_read_b64_tr_b16 v[130:131], v210 offset:0x3e00
	v_cvt_pk_f16_f32 v137, v138, v139
	v_add_f32_e32 v158, v158, v138
	v_add_f32_e32 v139, v159, v139
	v_mfma_f32_32x32x16_f16 v[48:63], a[248:251], a[152:155], v[48:63]
	s_mov_b32 s94, s63
	v_cvt_pk_f16_f32 v138, v244, v245
	v_add_f32_e32 v158, v158, v244
	v_add_f32_e32 v159, v139, v245
	v_mfma_f32_32x32x16_f16 v[32:47], a[248:251], a[184:187], v[32:47]
	s_mov_b32 s95, s77
	v_cvt_pk_f16_f32 v139, v246, v247
	v_add_f32_e32 v158, v158, v246
	v_add_f32_e32 v159, v159, v247
	v_mfma_f32_32x32x16_f16 v[112:127], a[220:223], a[156:159], v[112:127]
	s_mov_b32 s96, s65
	v_add_f32_e32 v158, v158, v64
	v_add_f32_e32 v159, v159, v65
	v_mfma_f32_32x32x16_f16 v[96:111], a[220:223], a[188:191], v[96:111]
	s_mov_b32 s97, s69
	v_add_f32_e32 v158, v158, v70
	v_add_f32_e32 v159, v159, v71
	v_mfma_f32_32x32x16_f16 v[48:63], a[252:255], a[156:159], v[48:63]
	s_mov_b32 s98, s66
	v_add_f32_e32 v158, v158, v152
	v_add_f32_e32 v159, v159, v153
	v_mfma_f32_32x32x16_f16 v[32:47], a[252:255], a[188:191], v[32:47]
	s_mov_b32 s99, s78
	v_add_f32_e32 v158, v158, v154
	v_add_f32_e32 v159, v159, v155
	s_nop 0
	s_nop 4
	v_add_f32_e32 v156, v156, v157
	s_waitcnt vmcnt(0) lgkmcnt(0)
	s_barrier
	s_nop 0
	v_mov_b32_e32 v157, v156
	s_nop 1
	v_permlane32_swap_b32_e32 v156, v157
	v_add_f32_e32 v156, v156, v157
	s_nop 0
	v_add_f32_e32 v233, v233, v156
	v_add_f32_e32 v156, v158, v159
	s_nop 0
	v_mov_b32_e32 v157, v156
	s_nop 1
	v_permlane32_swap_b32_e32 v156, v157
	v_add_f32_e32 v156, v156, v157
	s_nop 0
	v_add_f32_e32 v232, v232, v156
	s_nop 1
	v_mfma_f32_32x32x16_f16 a[0:15], v[184:187], v[168:171], a[0:15]
	s_nop 0
	v_mfma_f32_32x32x16_f16 a[16:31], v[184:187], v[196:199], a[16:31]
	ds_read_b128 a[192:195], v206 offset:0
	s_nop 0
	v_mfma_f32_32x32x16_f16 a[32:47], v[188:191], v[168:171], a[32:47]
	ds_read_b128 a[196:199], v207 offset:0
	s_nop 0
	v_mfma_f32_32x32x16_f16 a[48:63], v[188:191], v[196:199], a[48:63]
	ds_read_b128 a[200:203], v208 offset:0
	s_nop 0
	v_mfma_f32_32x32x16_f16 a[64:79], v[180:183], v[168:171], a[64:79]
	ds_read_b128 a[204:207], v209 offset:0
	s_nop 0
	v_mfma_f32_32x32x16_f16 a[80:95], v[180:183], v[196:199], a[80:95]
	ds_read_b128 a[208:211], v206 offset:128
	s_nop 0
	v_mfma_f32_32x32x16_f16 a[96:111], v[192:195], v[168:171], a[96:111]
	ds_read_b128 a[212:215], v207 offset:128
	s_nop 0
	v_mfma_f32_32x32x16_f16 a[112:127], v[192:195], v[196:199], a[112:127]
	ds_read_b128 a[216:219], v208 offset:128
	s_nop 0
	v_mfma_f32_32x32x16_f16 a[0:15], v[176:179], v[160:163], a[0:15]
	ds_read_b128 a[220:223], v209 offset:128
	v_max3_f32 v156, v112, v113, v48
	v_max3_f32 v157, v114, v115, v49
	s_nop 0
	v_max3_f32 v156, v156, v50, v51
	v_mfma_f32_32x32x16_f16 a[16:31], v[176:179], v[148:151], a[16:31]
	ds_read_b128 a[224:227], v206 offset:8192
	s_nop 0
	v_max3_f32 v156, v156, v116, v117
	v_max3_f32 v157, v157, v118, v119
	s_nop 0
	v_max3_f32 v156, v156, v52, v53
	v_max3_f32 v157, v157, v54, v55
	v_mfma_f32_32x32x16_f16 a[32:47], v[172:175], v[160:163], a[32:47]
	ds_read_b128 a[228:231], v207 offset:8192
	s_nop 0
	v_max3_f32 v156, v156, v120, v121
	v_max3_f32 v157, v157, v122, v123
	s_nop 0
	v_max3_f32 v156, v156, v56, v57
	v_max3_f32 v157, v157, v58, v59
	v_mfma_f32_32x32x16_f16 a[48:63], v[172:175], v[148:151], a[48:63]
	ds_read_b128 a[232:235], v208 offset:8192
	s_nop 0
	v_max3_f32 v156, v156, v124, v125
	v_max3_f32 v157, v157, v126, v127
	s_nop 0
	v_max3_f32 v156, v156, v60, v61
	v_max3_f32 v157, v157, v62, v63
	v_mfma_f32_32x32x16_f16 a[64:79], v[164:167], v[160:163], a[64:79]
	ds_read_b128 a[236:239], v209 offset:8192
	v_max3_f32 v158, v96, v97, v32
	v_max3_f32 v159, v98, v99, v33
	s_nop 0
	v_max3_f32 v158, v158, v34, v35
	v_mfma_f32_32x32x16_f16 a[80:95], v[164:167], v[148:151], a[80:95]
	ds_read_b128 a[240:243], v206 offset:8320
	s_nop 0
	v_max3_f32 v158, v158, v100, v101
	v_max3_f32 v159, v159, v102, v103
	s_nop 0
	v_max3_f32 v158, v158, v36, v37
	v_max3_f32 v159, v159, v38, v39
	v_mfma_f32_32x32x16_f16 a[96:111], v[144:147], v[160:163], a[96:111]
	ds_read_b128 a[244:247], v207 offset:8320
	s_nop 0
	v_max3_f32 v158, v158, v104, v105
	v_max3_f32 v159, v159, v106, v107
	s_nop 0
	v_max3_f32 v158, v158, v40, v41
	v_max3_f32 v159, v159, v42, v43
	v_mfma_f32_32x32x16_f16 a[112:127], v[144:147], v[148:151], a[112:127]
	ds_read_b128 a[248:251], v208 offset:8320
	s_nop 0
	v_max3_f32 v145, v159, v110, v111
	v_max3_f32 v144, v158, v108, v109
	s_nop 0
	v_max3_f32 v146, v144, v44, v45
	v_max3_f32 v145, v145, v46, v47
	v_mfma_f32_32x32x16_f16 a[0:15], v[140:143], v[72:75], a[0:15]
	ds_read_b128 a[252:255], v209 offset:8320
	v_max_f32_e32 v144, v156, v157
	s_nop 0
	v_mov_b32_e32 v147, v144
	s_nop 1
	v_permlane32_swap_b32_e32 v144, v147
	v_max_f32_e32 v144, v144, v147
	v_mfma_f32_32x32x16_f16 a[16:31], v[140:143], v[136:139], a[16:31]
	v_max_f32_e32 v140, v146, v145
	s_nop 0
	v_mov_b32_e32 v141, v140
	s_nop 1
	v_permlane32_swap_b32_e32 v140, v141
	v_max_f32_e32 v140, v140, v141
	v_max_f32_e32 v141, v144, v144
	v_max_f32_e32 v142, v140, v140
	v_max_f32_e32 v141, v141, v142
	v_mfma_f32_32x32x16_f16 a[32:47], v[66:69], v[72:75], a[32:47]
	v_cmp_lt_f32_e32 vcc, s79, v141
	s_cmp_lg_u64 vcc, 0
	s_cselect_b64 s[12:13], -1, 0
	s_cbranch_vccnz .LBB3_30

.LBB3_25:
	s_waitcnt lgkmcnt(0)
	s_add_u32 s12, s4, s34
	s_addc_u32 s13, s5, s35
	s_and_b32 s13, s13, 0xffff
	s_lshl_b32 s16, s24, 8
	ds_read_b64_tr_b16 v[156:157], v225 offset:0
	ds_read_b64_tr_b16 v[158:159], v225 offset:0x800
	ds_read_b64_tr_b16 v[152:153], v225 offset:0x200
	ds_read_b64_tr_b16 v[154:155], v225 offset:0xa00
	ds_read_b64_tr_b16 v[148:149], v225 offset:0x400
	ds_read_b64_tr_b16 v[150:151], v225 offset:0xc00
	ds_read_b64_tr_b16 v[144:145], v225 offset:0x600
	ds_read_b64_tr_b16 v[146:147], v225 offset:0xe00
	ds_read_b64_tr_b16 v[140:141], v225 offset:0x1000
	ds_read_b64_tr_b16 v[142:143], v225 offset:0x1800
	ds_read_b64_tr_b16 v[136:137], v225 offset:0x1200
	ds_read_b64_tr_b16 v[138:139], v225 offset:0x1a00
	ds_read_b64_tr_b16 v[132:133], v225 offset:0x1400
	ds_read_b64_tr_b16 v[134:135], v225 offset:0x1c00
	ds_read_b64_tr_b16 v[128:129], v225 offset:0x1600
	ds_read_b64_tr_b16 v[130:131], v225 offset:0x1e00
	ds_read_b64_tr_b16 v[124:125], v225 offset:0x2000
	ds_read_b64_tr_b16 v[126:127], v225 offset:0x2800
	ds_read_b64_tr_b16 v[120:121], v225 offset:0x2200
	v_exp_f32_e32 v164, v48
	v_exp_f32_e32 v173, v57
	v_cvt_pk_f16_f32 v57, v66, v67
	v_add_f32_e32 v66, v161, v164
	ds_read_b64_tr_b16 v[122:123], v225 offset:0x2a00
	v_exp_f32_e32 v165, v49
	v_exp_f32_e32 v166, v50
	v_add_f32_e32 v67, v160, v165
	v_add_f32_e32 v66, v66, v166
	ds_read_b64_tr_b16 v[116:117], v225 offset:0x2400
	v_exp_f32_e32 v167, v51
	v_exp_f32_e32 v168, v52
	v_exp_f32_e32 v60, v60
	v_exp_f32_e32 v61, v61
	v_add_f32_e32 v67, v67, v167
	v_add_f32_e32 v66, v66, v168
	ds_read_b64_tr_b16 v[118:119], v225 offset:0x2c00
	v_exp_f32_e32 v169, v53
	v_exp_f32_e32 v170, v54
	v_add_f32_e32 v67, v67, v169
	v_add_f32_e32 v66, v66, v170
	ds_read_b64_tr_b16 v[112:113], v225 offset:0x2600
	v_exp_f32_e32 v171, v55
	v_exp_f32_e32 v172, v56
	v_add_f32_e32 v67, v67, v171
	v_add_f32_e32 v66, v66, v172
	ds_read_b64_tr_b16 v[114:115], v225 offset:0x2e00
	v_exp_f32_e32 v174, v58
	v_add_f32_e32 v67, v67, v173
	v_add_f32_e32 v66, v66, v174
	ds_read_b64_tr_b16 v[108:109], v225 offset:0x3000
	v_exp_f32_e32 v175, v59
	v_exp_f32_e32 v178, v32
	v_exp_f32_e32 v180, v34
	v_cvt_pk_f16_f32 v34, v60, v61
	v_add_f32_e32 v67, v67, v175
	v_add_f32_e32 v60, v66, v60
	v_add_f32_e32 v66, v162, v178
	ds_read_b64_tr_b16 v[110:111], v225 offset:0x3800
	v_exp_f32_e32 v179, v33
	v_add_f32_e32 v61, v67, v61
	v_add_f32_e32 v67, v163, v179
	v_add_f32_e32 v66, v66, v180
	ds_read_b64_tr_b16 v[104:105], v225 offset:0x3200
	v_exp_f32_e32 v181, v35
	v_exp_f32_e32 v182, v36
	v_add_f32_e32 v67, v67, v181
	v_add_f32_e32 v66, v66, v182
	ds_read_b64_tr_b16 v[106:107], v225 offset:0x3a00
	v_exp_f32_e32 v183, v37
	v_exp_f32_e32 v184, v38
	v_add_f32_e32 v67, v67, v183
	v_add_f32_e32 v66, v66, v184
	ds_read_b64_tr_b16 v[100:101], v225 offset:0x3400
	v_exp_f32_e32 v176, v62
	v_exp_f32_e32 v177, v63
	v_exp_f32_e32 v185, v39
	v_exp_f32_e32 v186, v40
	v_add_f32_e32 v60, v60, v176
	v_add_f32_e32 v61, v61, v177
	v_add_f32_e32 v67, v67, v185
	v_add_f32_e32 v66, v66, v186
	ds_read_b64_tr_b16 v[102:103], v225 offset:0x3c00
	v_exp_f32_e32 v187, v41
	v_exp_f32_e32 v188, v42
	v_add_f32_e32 v67, v67, v187
	v_add_f32_e32 v66, v66, v188
	v_add_f32_e32 v60, v60, v61
	ds_read_b64_tr_b16 v[96:97], v225 offset:0x3600
	v_exp_f32_e32 v189, v43
	v_mov_b32_e32 v61, v60
	v_exp_f32_e32 v190, v44
	v_add_f32_e32 v67, v67, v189
	v_add_f32_e32 v66, v66, v190
	s_nop 0
	v_permlane32_swap_b32_e32 v60, v61
	ds_read_b64_tr_b16 v[98:99], v225 offset:0x3e00
	v_exp_f32_e32 v191, v45
	v_exp_f32_e32 v192, v46
	v_exp_f32_e32 v193, v47
	s_nop 1
	s_nop 1
	s_nop 1
	s_nop 1
	s_nop 1
	s_nop 1
	s_nop 1
	s_nop 1
	s_nop 1
	s_nop 1
	s_nop 1
	s_nop 1
	s_nop 1
	s_nop 1
	v_add_f32_e32 v67, v67, v191
	s_nop 1
	v_add_f32_e32 v66, v66, v192
	s_nop 1
	v_add_f32_e32 v60, v60, v61
	s_waitcnt lgkmcnt(0)
	v_cvt_pk_f16_f32 v56, v64, v65
	v_add_f32_e32 v67, v67, v193
	v_add_f32_e32 v61, v233, v60
	v_cvt_pk_f16_f32 v58, v68, v69
	v_add_f32_e32 v60, v66, v67
	v_cvt_pk_f16_f32 v59, v70, v71
	v_mov_b32_e32 v66, v60
	s_nop 1
	v_permlane32_swap_b32_e32 v60, v66
	v_add_f32_e32 v60, v60, v66
	v_cvt_pk_f16_f32 v44, v72, v73
	v_cvt_pk_f16_f32 v45, v74, v75
	v_cvt_pk_f16_f32 v46, v76, v77
	v_cvt_pk_f16_f32 v47, v78, v79
	v_cvt_pk_f16_f32 v62, v80, v81
	v_cvt_pk_f16_f32 v63, v82, v83
	v_cvt_pk_f16_f32 v64, v84, v85
	v_cvt_pk_f16_f32 v65, v86, v87
	v_cvt_pk_f16_f32 v52, v88, v89
	v_cvt_pk_f16_f32 v53, v90, v91
	v_cvt_pk_f16_f32 v54, v92, v93
	v_cvt_pk_f16_f32 v55, v94, v95
	v_cvt_pk_f16_f32 v40, v164, v165
	v_cvt_pk_f16_f32 v41, v166, v167
	v_cvt_pk_f16_f32 v42, v168, v169
	v_cvt_pk_f16_f32 v43, v170, v171
	v_cvt_pk_f16_f32 v32, v172, v173
	v_cvt_pk_f16_f32 v33, v174, v175
	v_cvt_pk_f16_f32 v35, v176, v177
	v_cvt_pk_f16_f32 v48, v178, v179
	v_cvt_pk_f16_f32 v49, v180, v181
	v_cvt_pk_f16_f32 v50, v182, v183
	v_cvt_pk_f16_f32 v51, v184, v185
	v_cvt_pk_f16_f32 v36, v186, v187
	v_cvt_pk_f16_f32 v37, v188, v189
	v_cvt_pk_f16_f32 v38, v190, v191
	v_cvt_pk_f16_f32 v39, v192, v193
	v_add_f32_e32 v60, v232, v60
	s_nop 1
	v_mfma_f32_32x32x16_f16 a[0:15], v[156:159], v[56:59], a[0:15]
	s_nop 0
	v_mfma_f32_32x32x16_f16 a[16:31], v[156:159], v[62:65], a[16:31]
	s_nop 0
	v_mfma_f32_32x32x16_f16 a[32:47], v[152:155], v[56:59], a[32:47]
	s_cmp_lg_u32 0, -1
	s_cselect_b32 s17, 0, 0
	s_add_i32 s17, s17, s89
	v_mfma_f32_32x32x16_f16 a[48:63], v[152:155], v[62:65], a[48:63]
	s_add_i32 s20, s17, 0x10400
	s_add_i32 s21, s16, 0x400
	v_mfma_f32_32x32x16_f16 a[64:79], v[148:151], v[56:59], a[64:79]
	s_nop 0
	v_mfma_f32_32x32x16_f16 a[80:95], v[148:151], v[62:65], a[80:95]
	s_add_i32 s20, s17, 0x10800
	s_add_i32 s21, s16, 0x800
	v_mfma_f32_32x32x16_f16 a[96:111], v[144:147], v[56:59], a[96:111]
	s_nop 0
	v_mfma_f32_32x32x16_f16 a[112:127], v[144:147], v[62:65], a[112:127]
	s_add_i32 s20, s17, 0x10c00
	s_add_i32 s21, s16, 0xc00
	v_mfma_f32_32x32x16_f16 a[0:15], v[140:143], v[44:47], a[0:15]
	s_nop 0
	v_mfma_f32_32x32x16_f16 a[16:31], v[140:143], v[52:55], a[16:31]
	s_add_i32 s20, s17, 0x11000
	s_add_i32 s21, s16, 0x1000
	v_mfma_f32_32x32x16_f16 a[32:47], v[136:139], v[44:47], a[32:47]
	s_nop 0
	v_mfma_f32_32x32x16_f16 a[48:63], v[136:139], v[52:55], a[48:63]
	s_add_i32 s20, s17, 0x11400
	s_add_i32 s21, s16, 0x1400
	v_mfma_f32_32x32x16_f16 a[64:79], v[132:135], v[44:47], a[64:79]
	s_nop 0
	v_mfma_f32_32x32x16_f16 a[80:95], v[132:135], v[52:55], a[80:95]
	s_add_i32 s20, s17, 0x11800
	s_add_i32 s21, s16, 0x1800
	v_mfma_f32_32x32x16_f16 a[96:111], v[128:131], v[44:47], a[96:111]
	s_nop 0
	v_mfma_f32_32x32x16_f16 a[112:127], v[128:131], v[52:55], a[112:127]
	s_add_i32 s20, s17, 0x11c00
	s_add_i32 s21, s16, 0x1c00
	v_mfma_f32_32x32x16_f16 a[0:15], v[124:127], v[40:43], a[0:15]
	s_nop 0
	v_mfma_f32_32x32x16_f16 a[16:31], v[124:127], v[48:51], a[16:31]
	s_add_i32 s20, s17, 0x12000
	s_add_i32 s21, s16, 0x2000
	v_mfma_f32_32x32x16_f16 a[32:47], v[120:123], v[40:43], a[32:47]
	s_nop 0
	v_mfma_f32_32x32x16_f16 a[48:63], v[120:123], v[48:51], a[48:63]
	s_add_i32 s20, s17, 0x12400
	s_add_i32 s21, s16, 0x2400
	v_mfma_f32_32x32x16_f16 a[64:79], v[116:119], v[40:43], a[64:79]
	s_nop 0
	v_mfma_f32_32x32x16_f16 a[80:95], v[116:119], v[48:51], a[80:95]
	s_add_i32 s20, s17, 0x12800
	s_add_i32 s21, s16, 0x2800
	v_mfma_f32_32x32x16_f16 a[96:111], v[112:115], v[40:43], a[96:111]
	s_nop 0
	v_mfma_f32_32x32x16_f16 a[112:127], v[112:115], v[48:51], a[112:127]
	s_add_i32 s20, s17, 0x12c00
	s_add_i32 s21, s16, 0x2c00
	v_mfma_f32_32x32x16_f16 a[0:15], v[108:111], v[32:35], a[0:15]
	s_nop 0
	v_mfma_f32_32x32x16_f16 a[16:31], v[108:111], v[36:39], a[16:31]
	s_add_i32 s20, s17, 0x13000
	s_add_i32 s21, s16, 0x3000
	v_mfma_f32_32x32x16_f16 a[32:47], v[104:107], v[32:35], a[32:47]
	s_nop 0
	v_mfma_f32_32x32x16_f16 a[48:63], v[104:107], v[36:39], a[48:63]
	s_add_i32 s20, s17, 0x13400
	s_add_i32 s21, s16, 0x3400
	v_mfma_f32_32x32x16_f16 a[64:79], v[100:103], v[32:35], a[64:79]
	s_nop 0
	v_mfma_f32_32x32x16_f16 a[80:95], v[100:103], v[36:39], a[80:95]
	s_add_i32 s20, s17, 0x13800
	s_add_i32 s21, s16, 0x3800
	v_mfma_f32_32x32x16_f16 a[96:111], v[96:99], v[32:35], a[96:111]
	s_nop 0
	v_mfma_f32_32x32x16_f16 a[112:127], v[96:99], v[36:39], a[112:127]
	s_add_i32 s17, s17, 0x13c00
	s_addk_i32 s16, 0x3c00
	s_lshl_b32 s12, s28, 8
	v_lshlrev_b32_e32 v32, 8, v227
	v_lshrrev_b32_e32 v33, 2, v227
	s_and_b32 s12, s12, 0xf00
	v_rcp_f32_e32 v37, v61
	v_lshrrev_b32_e32 v200, 4, v227
	v_and_b32_e32 v32, 0x1f00, v32
	v_and_b32_e32 v33, 0x3ffffff8, v33
	s_add_u32 s12, s10, s12
	v_add3_u32 v36, v216, v32, v33
	s_addc_u32 s13, s11, 0
	v_lshlrev_b64 v[32:33], 12, v[200:201]
	v_lshlrev_b32_e32 v34, 4, v227
	v_and_b32_e32 v34, 0xf0, v34
	v_mov_b32_e32 v35, v201
	v_lshl_add_u64 v[32:33], s[12:13], 0, v[32:33]
	v_cmp_lt_f32_e32 vcc, 0, v61
	s_nop 7
	s_nop 7
	v_lshl_add_u64 v[66:67], v[32:33], 0, v[34:35]
	v_add_u32_e32 v61, v36, v34
	v_cndmask_b32_e32 v35, 0, v37, vcc
	v_accvgpr_read_b32 v32, a0
	v_accvgpr_read_b32 v33, a1
	v_accvgpr_read_b32 v37, a2
	v_accvgpr_read_b32 v38, a3
	v_accvgpr_read_b32 v39, a4
	v_accvgpr_read_b32 v40, a5
	v_accvgpr_read_b32 v41, a6
	v_accvgpr_read_b32 v42, a7
	v_accvgpr_read_b32 v43, a8
	v_accvgpr_read_b32 v44, a9
	v_accvgpr_read_b32 v45, a10
	v_accvgpr_read_b32 v46, a11
	v_accvgpr_read_b32 v47, a12
	v_accvgpr_read_b32 v48, a13
	v_accvgpr_read_b32 v49, a14
	v_accvgpr_read_b32 v50, a15

	v_xad_u32 v70, v34, 16, v36
	v_mul_f32_e32 v32, v32, v35
	v_mul_f32_e32 v33, v33, v35
	v_xad_u32 v71, v34, 32, v36
	v_cvt_pk_f16_f32 v32, v32, v33
	v_mul_f32_e32 v33, v37, v35
	v_mul_f32_e32 v37, v38, v35
	v_xad_u32 v72, v34, 48, v36
	v_cvt_pk_f16_f32 v33, v33, v37
	ds_write_b64 v61, v[32:33]
	v_mul_f32_e32 v32, v39, v35
	v_mul_f32_e32 v33, v40, v35
	v_mul_f32_e32 v37, v42, v35
	v_xad_u32 v73, v34, 64, v36
	v_cvt_pk_f16_f32 v32, v32, v33
	v_mul_f32_e32 v33, v41, v35
	s_movk_i32 s12, 0x50
	v_cvt_pk_f16_f32 v33, v33, v37
	ds_write_b64 v70, v[32:33]
	v_mul_f32_e32 v32, v43, v35
	v_mul_f32_e32 v33, v44, v35
	v_mul_f32_e32 v37, v46, v35
	v_xad_u32 v74, v34, s12, v36
	v_cvt_pk_f16_f32 v32, v32, v33
	v_mul_f32_e32 v33, v45, v35
	s_movk_i32 s12, 0x60
	v_cvt_pk_f16_f32 v33, v33, v37
	ds_write_b64 v71, v[32:33]
	v_mul_f32_e32 v32, v47, v35
	v_mul_f32_e32 v33, v48, v35
	v_mul_f32_e32 v37, v50, v35
	v_xad_u32 v75, v34, s12, v36
	v_cvt_pk_f16_f32 v32, v32, v33
	v_mul_f32_e32 v33, v49, v35
	s_movk_i32 s12, 0x70
	v_cvt_pk_f16_f32 v33, v33, v37
	ds_write_b64 v72, v[32:33]
	v_accvgpr_read_b32 v32, a32
	v_accvgpr_read_b32 v33, a33
	v_accvgpr_read_b32 v37, a34
	v_accvgpr_read_b32 v38, a35
	v_accvgpr_read_b32 v39, a36
	v_accvgpr_read_b32 v40, a37
	v_accvgpr_read_b32 v41, a38
	v_accvgpr_read_b32 v42, a39
	v_accvgpr_read_b32 v43, a40
	v_accvgpr_read_b32 v44, a41
	v_accvgpr_read_b32 v45, a42
	v_accvgpr_read_b32 v46, a43
	v_accvgpr_read_b32 v47, a44
	v_accvgpr_read_b32 v48, a45
	v_accvgpr_read_b32 v49, a46
	v_accvgpr_read_b32 v50, a47

	v_xad_u32 v76, v34, s12, v36
	v_mul_f32_e32 v32, v32, v35
	v_mul_f32_e32 v33, v33, v35
	s_movk_i32 s12, 0x80
	v_cvt_pk_f16_f32 v32, v32, v33
	v_mul_f32_e32 v33, v37, v35
	v_mul_f32_e32 v37, v38, v35
	v_xad_u32 v77, v34, s12, v36
	v_cvt_pk_f16_f32 v33, v33, v37
	ds_write_b64 v73, v[32:33]
	v_mul_f32_e32 v32, v39, v35
	v_mul_f32_e32 v33, v40, v35
	v_mul_f32_e32 v37, v42, v35
	s_movk_i32 s12, 0x90
	v_cvt_pk_f16_f32 v32, v32, v33
	v_mul_f32_e32 v33, v41, v35
	v_xad_u32 v78, v34, s12, v36
	v_cvt_pk_f16_f32 v33, v33, v37
	ds_write_b64 v74, v[32:33]
	v_mul_f32_e32 v32, v43, v35
	v_mul_f32_e32 v33, v44, v35
	v_mul_f32_e32 v37, v46, v35
	s_movk_i32 s12, 0xa0
	v_cvt_pk_f16_f32 v32, v32, v33
	v_mul_f32_e32 v33, v45, v35
	v_xad_u32 v79, v34, s12, v36
	v_cvt_pk_f16_f32 v33, v33, v37
	ds_write_b64 v75, v[32:33]
	v_mul_f32_e32 v32, v47, v35
	v_mul_f32_e32 v33, v48, v35
	v_mul_f32_e32 v37, v50, v35
	s_movk_i32 s12, 0xb0
	v_cvt_pk_f16_f32 v32, v32, v33
	v_mul_f32_e32 v33, v49, v35
	v_xad_u32 v80, v34, s12, v36
	v_cvt_pk_f16_f32 v33, v33, v37
	ds_write_b64 v76, v[32:33]
	v_accvgpr_read_b32 v32, a64
	v_accvgpr_read_b32 v33, a65
	v_accvgpr_read_b32 v37, a66
	v_accvgpr_read_b32 v38, a67
	v_accvgpr_read_b32 v39, a68
	v_accvgpr_read_b32 v40, a69
	v_accvgpr_read_b32 v41, a70
	v_accvgpr_read_b32 v42, a71
	v_accvgpr_read_b32 v43, a72
	v_accvgpr_read_b32 v44, a73
	v_accvgpr_read_b32 v45, a74
	v_accvgpr_read_b32 v46, a75
	v_accvgpr_read_b32 v47, a76
	v_accvgpr_read_b32 v48, a77
	v_accvgpr_read_b32 v49, a78
	v_accvgpr_read_b32 v50, a79

	s_movk_i32 s12, 0xc0
	v_mul_f32_e32 v32, v32, v35
	v_mul_f32_e32 v33, v33, v35
	v_xad_u32 v81, v34, s12, v36
	v_cvt_pk_f16_f32 v32, v32, v33
	v_mul_f32_e32 v33, v37, v35
	v_mul_f32_e32 v37, v38, v35
	v_xad_u32 v82, v34, s81, v36
	v_cvt_pk_f16_f32 v33, v33, v37
	ds_write_b64 v77, v[32:33]
	v_mul_f32_e32 v32, v39, v35
	v_mul_f32_e32 v33, v40, v35
	v_mul_f32_e32 v37, v42, v35
	v_xad_u32 v83, v34, s82, v36
	v_cvt_pk_f16_f32 v32, v32, v33
	v_mul_f32_e32 v33, v41, v35
	s_movk_i32 s12, 0xf0
	v_cvt_pk_f16_f32 v33, v33, v37
	ds_write_b64 v78, v[32:33]
	v_mul_f32_e32 v32, v43, v35
	v_mul_f32_e32 v33, v44, v35
	v_mul_f32_e32 v37, v46, v35
	v_xad_u32 v84, v34, s12, v36
	v_cvt_pk_f16_f32 v32, v32, v33
	v_mul_f32_e32 v33, v45, v35
	v_add_u32_e32 v56, 24, v200
	v_cvt_pk_f16_f32 v33, v33, v37
	ds_write_b64 v79, v[32:33]
	v_mul_f32_e32 v32, v47, v35
	v_mul_f32_e32 v33, v48, v35
	v_mul_f32_e32 v37, v50, v35
	v_lshlrev_b32_e32 v57, 8, v56
	v_cvt_pk_f16_f32 v32, v32, v33
	v_mul_f32_e32 v33, v49, v35
	v_xor_b32_e32 v56, v56, v227
	v_cvt_pk_f16_f32 v33, v33, v37
	ds_write_b64 v80, v[32:33]
	v_accvgpr_read_b32 v32, a96
	v_accvgpr_read_b32 v33, a97
	v_accvgpr_read_b32 v37, a98
	v_accvgpr_read_b32 v38, a99
	v_accvgpr_read_b32 v39, a100
	v_accvgpr_read_b32 v40, a101
	v_accvgpr_read_b32 v41, a102
	v_accvgpr_read_b32 v42, a103
	v_accvgpr_read_b32 v43, a104
	v_accvgpr_read_b32 v44, a105
	v_accvgpr_read_b32 v45, a106
	v_accvgpr_read_b32 v46, a107
	v_accvgpr_read_b32 v47, a108
	v_accvgpr_read_b32 v48, a109
	v_accvgpr_read_b32 v49, a110
	v_accvgpr_read_b32 v50, a111

	v_lshlrev_b32_e32 v56, 4, v56
	v_mul_f32_e32 v32, v32, v35
	v_mul_f32_e32 v33, v33, v35
	v_and_b32_e32 v56, 0xf0, v56
	v_cvt_pk_f16_f32 v32, v32, v33
	v_mul_f32_e32 v33, v37, v35
	v_mul_f32_e32 v37, v38, v35
	v_add3_u32 v90, v216, v57, v56
	v_cvt_pk_f16_f32 v33, v33, v37
	ds_write_b64 v81, v[32:33]
	v_mul_f32_e32 v32, v39, v35
	v_mul_f32_e32 v33, v40, v35
	v_mul_f32_e32 v37, v42, v35
	v_add_u32_e32 v40, 12, v200
	v_cvt_pk_f16_f32 v32, v32, v33
	v_mul_f32_e32 v33, v41, v35
	v_lshlrev_b32_e32 v41, 8, v40
	v_cvt_pk_f16_f32 v33, v33, v37
	ds_write_b64 v82, v[32:33]
	v_mul_f32_e32 v32, v43, v35
	v_mul_f32_e32 v33, v44, v35
	v_mul_f32_e32 v37, v46, v35
	v_xor_b32_e32 v40, v40, v227
	v_cvt_pk_f16_f32 v32, v32, v33
	v_mul_f32_e32 v33, v45, v35
	v_lshlrev_b32_e32 v40, 4, v40
	v_cvt_pk_f16_f32 v33, v33, v37
	ds_write_b64 v83, v[32:33]
	v_mul_f32_e32 v32, v47, v35
	v_mul_f32_e32 v33, v48, v35
	v_and_b32_e32 v40, 0xf0, v40
	v_cvt_pk_f16_f32 v32, v32, v33
	v_mul_f32_e32 v33, v49, v35
	v_mul_f32_e32 v35, v50, v35
	v_add3_u32 v88, v216, v41, v40
	v_cvt_pk_f16_f32 v33, v33, v35
	ds_write_b64 v84, v[32:33]
	v_xor_b32_e32 v33, v200, v227
	v_lshlrev_b32_e32 v33, 4, v33
	v_lshlrev_b32_e32 v32, 8, v200
	v_and_b32_e32 v33, 0xf0, v33
	v_add3_u32 v85, v216, v32, v33
	v_add_u32_e32 v32, 4, v200
	v_lshlrev_b32_e32 v33, 8, v32
	v_xor_b32_e32 v32, v32, v227
	v_lshlrev_b32_e32 v32, 4, v32
	v_and_b32_e32 v32, 0xf0, v32
	v_add3_u32 v86, v216, v33, v32
	v_add_u32_e32 v32, 8, v200
	v_lshlrev_b32_e32 v33, 8, v32
	v_xor_b32_e32 v32, v32, v227
	v_lshlrev_b32_e32 v32, 4, v32
	s_waitcnt lgkmcnt(0)
	v_and_b32_e32 v32, 0xf0, v32
	v_add3_u32 v87, v216, v33, v32
	ds_read_b128 v[32:35], v86
	ds_read_b128 v[36:39], v87
	ds_read_b128 v[40:43], v85
	ds_read_b128 v[44:47], v85 offset:4096
	v_add_u32_e32 v48, 20, v200
	v_add_u32_e32 v56, 28, v200
	v_lshlrev_b32_e32 v49, 8, v48
	v_xor_b32_e32 v48, v48, v227
	v_lshlrev_b32_e32 v57, 8, v56
	v_xor_b32_e32 v56, v56, v227
	v_lshlrev_b32_e32 v48, 4, v48
	v_lshlrev_b32_e32 v56, 4, v56
	v_lshl_or_b32 v68, v228, 12, s26
	v_mov_b32_e32 v69, s27
	v_and_b32_e32 v48, 0xf0, v48
	v_and_b32_e32 v56, 0xf0, v56
	v_lshl_add_u64 v[66:67], v[66:67], 0, v[68:69]
	s_movk_i32 s12, 0x4000
	v_add3_u32 v89, v216, v49, v48
	ds_read_b128 v[48:51], v88
	ds_read_b128 v[52:55], v89
	v_add3_u32 v91, v216, v57, v56
	ds_read_b128 v[56:59], v90
	ds_read_b128 v[62:65], v91
	s_waitcnt lgkmcnt(5)
	global_store_dwordx4 v[66:67], v[40:43], off sc0 sc1
	s_mov_b64 s[28:29], s[30:31]
	s_nop 0
	v_add_co_u32_e32 v40, vcc, s12, v66
	s_mov_b32 s12, 0xc000
	s_nop 0
	v_addc_co_u32_e32 v41, vcc, 0, v67, vcc
	global_store_dwordx4 v[40:41], v[32:35], off sc0 sc1
	s_nop 1
	v_add_co_u32_e32 v32, vcc, s37, v66
	v_rcp_f32_e32 v34, v60
	s_nop 0
	v_addc_co_u32_e32 v33, vcc, 0, v67, vcc
	global_store_dwordx4 v[32:33], v[36:39], off sc0 sc1
	v_add_co_u32_e32 v32, vcc, s12, v66
	s_mov_b32 s12, 0x10000
	s_nop 0
	v_addc_co_u32_e32 v33, vcc, 0, v67, vcc
	s_waitcnt lgkmcnt(3)
	global_store_dwordx4 v[32:33], v[48:51], off sc0 sc1
	v_add_co_u32_e32 v32, vcc, s12, v66
	s_mov_b32 s12, 0x14000
	s_nop 0
	v_addc_co_u32_e32 v33, vcc, 0, v67, vcc
	global_store_dwordx4 v[32:33], v[44:47], off sc0 sc1
	v_add_co_u32_e32 v32, vcc, s12, v66
	s_nop 1
	v_addc_co_u32_e32 v33, vcc, 0, v67, vcc
	s_waitcnt lgkmcnt(2)
	global_store_dwordx4 v[32:33], v[52:55], off sc0 sc1
	v_add_co_u32_e32 v32, vcc, s83, v66
	s_nop 1
	v_addc_co_u32_e32 v33, vcc, 0, v67, vcc
	s_waitcnt lgkmcnt(1)
	global_store_dwordx4 v[32:33], v[56:59], off sc0 sc1
	v_add_co_u32_e32 v32, vcc, s84, v66
	s_nop 1
	v_addc_co_u32_e32 v33, vcc, 0, v67, vcc
	s_waitcnt lgkmcnt(0)
	global_store_dwordx4 v[32:33], v[62:65], off sc0 sc1
	s_waitcnt lgkmcnt(0)
	v_cmp_lt_f32_e32 vcc, 0, v60
	v_accvgpr_read_b32 v32, a16
	v_accvgpr_read_b32 v33, a17
	v_accvgpr_read_b32 v35, a18
	v_accvgpr_read_b32 v36, a19
	v_accvgpr_read_b32 v37, a20
	v_accvgpr_read_b32 v38, a21
	v_accvgpr_read_b32 v39, a22
	v_accvgpr_read_b32 v40, a23
	v_accvgpr_read_b32 v41, a24
	v_accvgpr_read_b32 v42, a25
	v_accvgpr_read_b32 v43, a26
	v_accvgpr_read_b32 v44, a27
	v_accvgpr_read_b32 v45, a28
	v_accvgpr_read_b32 v46, a29
	v_accvgpr_read_b32 v47, a30
	v_accvgpr_read_b32 v48, a31

	s_nop 1
	v_cndmask_b32_e32 v34, 0, v34, vcc
	v_mul_f32_e32 v32, v32, v34
	v_mul_f32_e32 v33, v33, v34
	v_add_co_u32_e32 v64, vcc, s15, v66
	v_cvt_pk_f16_f32 v32, v32, v33
	v_mul_f32_e32 v33, v35, v34
	v_mul_f32_e32 v35, v36, v34
	s_nop 0
	v_addc_co_u32_e32 v65, vcc, 0, v67, vcc
	v_cvt_pk_f16_f32 v33, v33, v35
	ds_write_b64 v61, v[32:33]
	v_mul_f32_e32 v32, v37, v34
	v_mul_f32_e32 v33, v38, v34
	v_mul_f32_e32 v35, v40, v34
	s_nop 0
	v_cvt_pk_f16_f32 v32, v32, v33
	v_mul_f32_e32 v33, v39, v34
	s_nop 0
	v_cvt_pk_f16_f32 v33, v33, v35
	ds_write_b64 v70, v[32:33]
	v_mul_f32_e32 v32, v41, v34
	v_mul_f32_e32 v33, v42, v34
	v_mul_f32_e32 v35, v44, v34
	s_nop 0
	v_cvt_pk_f16_f32 v32, v32, v33
	v_mul_f32_e32 v33, v43, v34
	s_nop 0
	v_cvt_pk_f16_f32 v33, v33, v35
	ds_write_b64 v71, v[32:33]
	v_mul_f32_e32 v32, v45, v34
	v_mul_f32_e32 v33, v46, v34
	v_mul_f32_e32 v35, v48, v34
	s_nop 0
	v_cvt_pk_f16_f32 v32, v32, v33
	v_mul_f32_e32 v33, v47, v34
	s_nop 0
	v_cvt_pk_f16_f32 v33, v33, v35
	ds_write_b64 v72, v[32:33]
	v_accvgpr_read_b32 v32, a48
	v_accvgpr_read_b32 v33, a49
	v_accvgpr_read_b32 v35, a50
	v_accvgpr_read_b32 v36, a51
	v_accvgpr_read_b32 v37, a52
	v_accvgpr_read_b32 v38, a53
	v_accvgpr_read_b32 v39, a54
	v_accvgpr_read_b32 v40, a55
	v_accvgpr_read_b32 v41, a56
	v_accvgpr_read_b32 v42, a57
	v_accvgpr_read_b32 v43, a58
	v_accvgpr_read_b32 v44, a59
	v_accvgpr_read_b32 v45, a60
	v_accvgpr_read_b32 v46, a61
	v_accvgpr_read_b32 v47, a62
	v_accvgpr_read_b32 v48, a63

	s_nop 0
	v_mul_f32_e32 v32, v32, v34
	v_mul_f32_e32 v33, v33, v34
	s_nop 0
	v_cvt_pk_f16_f32 v32, v32, v33
	v_mul_f32_e32 v33, v35, v34
	v_mul_f32_e32 v35, v36, v34
	s_nop 0
	v_cvt_pk_f16_f32 v33, v33, v35
	ds_write_b64 v73, v[32:33]
	v_mul_f32_e32 v32, v37, v34
	v_mul_f32_e32 v33, v38, v34
	v_mul_f32_e32 v35, v40, v34
	s_nop 0
	v_cvt_pk_f16_f32 v32, v32, v33
	v_mul_f32_e32 v33, v39, v34
	s_nop 0
	v_cvt_pk_f16_f32 v33, v33, v35
	ds_write_b64 v74, v[32:33]
	v_mul_f32_e32 v32, v41, v34
	v_mul_f32_e32 v33, v42, v34
	v_mul_f32_e32 v35, v44, v34
	s_nop 0
	v_cvt_pk_f16_f32 v32, v32, v33
	v_mul_f32_e32 v33, v43, v34
	s_nop 0
	v_cvt_pk_f16_f32 v33, v33, v35
	ds_write_b64 v75, v[32:33]
	v_mul_f32_e32 v32, v45, v34
	v_mul_f32_e32 v33, v46, v34
	v_mul_f32_e32 v35, v48, v34
	s_nop 0
	v_cvt_pk_f16_f32 v32, v32, v33
	v_mul_f32_e32 v33, v47, v34
	s_nop 0
	v_cvt_pk_f16_f32 v33, v33, v35
	ds_write_b64 v76, v[32:33]
	v_accvgpr_read_b32 v32, a80
	v_accvgpr_read_b32 v33, a81
	v_accvgpr_read_b32 v35, a82
	v_accvgpr_read_b32 v36, a83
	v_accvgpr_read_b32 v37, a84
	v_accvgpr_read_b32 v38, a85
	v_accvgpr_read_b32 v39, a86
	v_accvgpr_read_b32 v40, a87
	v_accvgpr_read_b32 v41, a88
	v_accvgpr_read_b32 v42, a89
	v_accvgpr_read_b32 v43, a90
	v_accvgpr_read_b32 v44, a91
	v_accvgpr_read_b32 v45, a92
	v_accvgpr_read_b32 v46, a93
	v_accvgpr_read_b32 v47, a94
	v_accvgpr_read_b32 v48, a95

	s_nop 0
	v_mul_f32_e32 v32, v32, v34
	v_mul_f32_e32 v33, v33, v34
	s_nop 0
	v_cvt_pk_f16_f32 v32, v32, v33
	v_mul_f32_e32 v33, v35, v34
	v_mul_f32_e32 v35, v36, v34
	s_nop 0
	v_cvt_pk_f16_f32 v33, v33, v35
	ds_write_b64 v77, v[32:33]
	v_mul_f32_e32 v32, v37, v34
	v_mul_f32_e32 v33, v38, v34
	v_mul_f32_e32 v35, v40, v34
	s_nop 0
	v_cvt_pk_f16_f32 v32, v32, v33
	v_mul_f32_e32 v33, v39, v34
	s_nop 0
	v_cvt_pk_f16_f32 v33, v33, v35
	ds_write_b64 v78, v[32:33]
	v_mul_f32_e32 v32, v41, v34
	v_mul_f32_e32 v33, v42, v34
	v_mul_f32_e32 v35, v44, v34
	s_nop 0
	v_cvt_pk_f16_f32 v32, v32, v33
	v_mul_f32_e32 v33, v43, v34
	s_nop 0
	v_cvt_pk_f16_f32 v33, v33, v35
	ds_write_b64 v79, v[32:33]
	v_mul_f32_e32 v32, v45, v34
	v_mul_f32_e32 v33, v46, v34
	v_mul_f32_e32 v35, v48, v34
	s_nop 0
	v_cvt_pk_f16_f32 v32, v32, v33
	v_mul_f32_e32 v33, v47, v34
	s_nop 0
	v_cvt_pk_f16_f32 v33, v33, v35
	ds_write_b64 v80, v[32:33]
	v_accvgpr_read_b32 v32, a112
	v_accvgpr_read_b32 v33, a113
	v_accvgpr_read_b32 v35, a114
	v_accvgpr_read_b32 v36, a115
	v_accvgpr_read_b32 v37, a116
	v_accvgpr_read_b32 v38, a117
	v_accvgpr_read_b32 v39, a118
	v_accvgpr_read_b32 v40, a119
	v_accvgpr_read_b32 v41, a120
	v_accvgpr_read_b32 v42, a121
	v_accvgpr_read_b32 v43, a122
	v_accvgpr_read_b32 v44, a123
	v_accvgpr_read_b32 v45, a124
	v_accvgpr_read_b32 v46, a125
	v_accvgpr_read_b32 v47, a126
	v_accvgpr_read_b32 v48, a127

	s_nop 0
	v_mul_f32_e32 v32, v32, v34
	v_mul_f32_e32 v33, v33, v34
	s_nop 0
	v_cvt_pk_f16_f32 v32, v32, v33
	v_mul_f32_e32 v33, v35, v34
	v_mul_f32_e32 v35, v36, v34
	s_nop 0
	v_cvt_pk_f16_f32 v33, v33, v35
	ds_write_b64 v81, v[32:33]
	v_mul_f32_e32 v32, v37, v34
	v_mul_f32_e32 v33, v38, v34
	v_mul_f32_e32 v35, v40, v34
	s_nop 0
	v_cvt_pk_f16_f32 v32, v32, v33
	v_mul_f32_e32 v33, v39, v34
	s_nop 0
	v_cvt_pk_f16_f32 v33, v33, v35
	ds_write_b64 v82, v[32:33]
	v_mul_f32_e32 v32, v41, v34
	v_mul_f32_e32 v33, v42, v34
	v_mul_f32_e32 v35, v44, v34
	s_nop 0
	v_cvt_pk_f16_f32 v32, v32, v33
	v_mul_f32_e32 v33, v43, v34
	s_nop 0
	v_cvt_pk_f16_f32 v33, v33, v35
	ds_write_b64 v83, v[32:33]
	v_mul_f32_e32 v32, v45, v34
	v_mul_f32_e32 v33, v46, v34
	s_nop 0
	v_cvt_pk_f16_f32 v32, v32, v33
	v_mul_f32_e32 v33, v47, v34
	v_mul_f32_e32 v34, v48, v34
	s_nop 0
	v_cvt_pk_f16_f32 v33, v33, v34
	ds_write_b64 v84, v[32:33]
	s_waitcnt lgkmcnt(0)
	ds_read_b128 v[32:35], v86
	ds_read_b128 v[36:39], v87
	ds_read_b128 v[40:43], v85
	ds_read_b128 v[44:47], v85 offset:4096
	ds_read_b128 v[48:51], v88
	ds_read_b128 v[52:55], v89
	ds_read_b128 v[56:59], v90
	ds_read_b128 v[60:63], v91
	s_waitcnt lgkmcnt(5)
	global_store_dwordx4 v[64:65], v[40:43], off sc0 sc1
	s_nop 1
	v_add_co_u32_e32 v40, vcc, s85, v66
	s_nop 1
	v_addc_co_u32_e32 v41, vcc, 0, v67, vcc
	global_store_dwordx4 v[40:41], v[32:35], off sc0 sc1
	s_nop 1
	v_add_co_u32_e32 v32, vcc, s86, v66
	s_nop 1
	v_addc_co_u32_e32 v33, vcc, 0, v67, vcc
	global_store_dwordx4 v[32:33], v[36:39], off sc0 sc1
	v_add_co_u32_e32 v32, vcc, s87, v66
	s_nop 1
	v_addc_co_u32_e32 v33, vcc, 0, v67, vcc
	s_waitcnt lgkmcnt(3)
	global_store_dwordx4 v[32:33], v[48:51], off sc0 sc1
	v_add_co_u32_e32 v32, vcc, s88, v66
	s_nop 1
	v_addc_co_u32_e32 v33, vcc, 0, v67, vcc
	global_store_dwordx4 v[32:33], v[44:47], off sc0 sc1
	v_add_co_u32_e32 v32, vcc, 0x34000, v66
	s_nop 1
	v_addc_co_u32_e32 v33, vcc, 0, v67, vcc
	s_waitcnt lgkmcnt(2)
	global_store_dwordx4 v[32:33], v[52:55], off sc0 sc1
	v_add_co_u32_e32 v32, vcc, 0x38000, v66
	s_nop 1
	v_addc_co_u32_e32 v33, vcc, 0, v67, vcc
	s_waitcnt lgkmcnt(1)
	global_store_dwordx4 v[32:33], v[56:59], off sc0 sc1
	v_add_co_u32_e32 v32, vcc, 0x3c000, v66
	s_nop 1
	v_addc_co_u32_e32 v33, vcc, 0, v67, vcc
	s_waitcnt lgkmcnt(0)
	global_store_dwordx4 v[32:33], v[60:63], off sc0 sc1
	s_waitcnt lgkmcnt(0)
	s_and_b64 vcc, exec, s[0:1]
	s_cbranch_vccz .LBB3_2
	s_branch .LBB3_32
